# FT also warms the f16 feats of its batch (k_final's fragments) in L2
# baseline (speedup 1.0000x reference)
_Z6k_iterILb0ELb1EEvPKfS1_PKiPK15HIP_vector_typeIfLj4EES7_S1_S1_S3_S1_PfS8_S1_S3_PDF16_PS5_SA_PiSA_SB_:
	s_load_dwordx2 s[8:9], s[0:1], 0x80
	s_load_dwordx4 s[4:7], s[0:1], 0x70
	s_load_dwordx4 s[16:19], s[0:1], 0x40
	s_load_dwordx2 s[22:23], s[0:1], 0x50
	s_load_dwordx2 s[44:45], s[0:1], 0x68
	v_readfirstlane_b32 s12, v0
	v_cmp_gt_u32_e64 s[14:15], 64, v0
	v_lshlrev_b32_e32 v1, 2, v0
	s_and_saveexec_b64 s[10:11], s[14:15]
	v_mov_b32_e32 v2, 0
	ds_write_b32 v1, v2 offset:5152
	s_or_b64 exec, exec, s[10:11]
	s_lshl_b32 s3, s2, 5
	s_and_b32 s3, s3, 0xe0
	s_lshr_b32 s2, s2, 3
	s_add_i32 s2, s3, s2
	s_lshl_b32 s29, s2, 6
	v_and_b32_e32 v2, 31, v0
	v_or_b32_e32 v4, s29, v2
	v_mov_b32_e32 v5, 0
	s_lshr_b32 s30, s12, 6
	s_lshl_b32 s32, s30, 2
	s_lshr_b32 s32, 0x73261540, s32
	s_lshl_b32 s32, s32, 5
	s_and_b32 s32, s32, 0xe0
	v_or_b32_e32 v176, s32, v2
	v_lshlrev_b32_e32 v177, 4, v176
	v_add_u32_e32 v178, 0x1000, v177
	v_add_u32_e32 v179, 0x2000, v177
	v_add_u32_e32 v180, 0x3000, v177
	v_add_u32_e32 v181, 0x4000, v177
	v_add_u32_e32 v182, 0x5000, v177
	s_mov_b32 s3, 0
	s_lshl_b64 s[34:35], s[2:3], 16
	s_lshl_b32 s33, s2, 2
	s_waitcnt lgkmcnt(0)
	s_load_dword s26, s[8:9], s33 offset:0x0
	s_add_u32 s20, s4, s34
	s_addc_u32 s21, s5, s35
	v_lshl_add_u64 v[4:5], v[4:5], 4, s[6:7]
	global_load_dwordx3 v[30:32], v[4:5], off
	global_load_dwordx3 v[26:28], v[4:5], off offset:512
	global_load_dwordx4 v[2:5], v177, s[20:21]
	global_load_dwordx4 v[6:9], v178, s[20:21]
	global_load_dwordx4 v[10:13], v179, s[20:21]
	global_load_dwordx4 v[14:17], v180, s[20:21]
	global_load_dwordx4 v[18:21], v181, s[20:21]
	global_load_dwordx4 v[22:25], v182, s[20:21]
	v_and_b32_e32 v38, 63, v0
	v_mov_b32_e32 v29, 0xff800000
	v_cmp_gt_u32_e64 s[0:1], 32, v38
	s_waitcnt lgkmcnt(0)
	s_cmpk_gt_i32 s26, 0x600
	s_cselect_b64 s[24:25], -1, 0
	s_cmpk_lt_i32 s26, 0x601
	s_cbranch_scc1 .LBB4_6
	s_and_saveexec_b64 s[8:9], s[14:15]
	s_cbranch_execz .LBB4_5
	v_or_b32_e32 v178, s29, v0
	v_mov_b32_e32 v179, 0
	v_lshl_add_u64 v[178:179], v[178:179], 4, s[6:7]
	global_load_dwordx4 v[178:181], v[178:179], off
	v_lshlrev_b32_e32 v177, 4, v0
	s_waitcnt vmcnt(0)
	ds_write_b128 v177, v[178:181] offset:2080

.LBB4_39:
	s_waitcnt vmcnt(5)
	v_rcp_f32_e32 v2, v133
	s_waitcnt vmcnt(4)
	v_rcp_f32_e32 v3, v132
	s_waitcnt vmcnt(3)
	v_rcp_f32_e32 v4, v131
	v_cmp_lt_f32_e32 vcc, 0, v133
	s_waitcnt vmcnt(2)
	v_rcp_f32_e32 v5, v130
	s_waitcnt vmcnt(1)
	v_rcp_f32_e32 v6, v129
	v_cndmask_b32_e32 v2, 0, v2, vcc
	v_cmp_lt_f32_e32 vcc, 0, v132
	s_waitcnt vmcnt(0)
	v_rcp_f32_e32 v7, v128
	s_getpc_b64 s[36:37]
	s_sub_u32 s36, s36, 0x9034
	s_subb_u32 s37, s37, 0
	v_lshlrev_b32_e32 v183, 6, v0
	v_min_u32_e32 v183, 0x1980, v183
	global_load_dword v183, v183, s[36:37]
	s_lshr_b32 s46, s29, 12
	s_lshl_b32 s46, s46, 19
	s_bfe_u32 s47, s29, 0x50006
	s_lshl_b32 s47, s47, 14
	s_add_i32 s46, s46, s47
	s_and_b32 s46, s46, 0x1fc000
	s_add_u32 s46, s44, s46
	s_addc_u32 s47, s45, 0
	v_lshlrev_b32_e32 v182, 5, v0
	v_and_b32_e32 v182, 0x3fe0, v182
	global_load_dword v182, v182, s[46:47]
	s_mov_b32 s4, 0x42c80000
	v_cndmask_b32_e32 v3, 0, v3, vcc
	v_cmp_lt_f32_e32 vcc, 0, v131
	v_cmp_ngt_f32_e64 s[2:3], s4, v3
	s_mov_b64 s[6:7], 0
	v_cndmask_b32_e32 v4, 0, v4, vcc
	v_cmp_lt_f32_e32 vcc, 0, v130
	s_nop 1
	v_cndmask_b32_e32 v5, 0, v5, vcc
	v_cmp_lt_f32_e32 vcc, 0, v129
	s_nop 1
	v_cndmask_b32_e32 v6, 0, v6, vcc
	v_cmp_lt_f32_e32 vcc, 0, v128
	s_nop 1
	v_cndmask_b32_e32 v7, 0, v7, vcc
	v_cmp_ngt_f32_e32 vcc, s4, v2
	s_or_b64 s[2:3], vcc, s[2:3]
	v_cmp_ngt_f32_e32 vcc, s4, v4
	s_or_b64 s[2:3], s[2:3], vcc
	v_cmp_ngt_f32_e32 vcc, s4, v5
	s_or_b64 s[2:3], s[2:3], vcc
	v_cmp_ngt_f32_e32 vcc, s4, v6
	s_or_b64 s[2:3], s[2:3], vcc
	v_cmp_ngt_f32_e32 vcc, s4, v7
	s_or_b64 s[2:3], s[2:3], vcc
	v_cndmask_b32_e64 v8, 0, 1, s[2:3]
	v_cmp_ne_u32_e32 vcc, 0, v8
	s_cmp_eq_u64 vcc, 0
	s_cselect_b64 s[2:3], -1, 0
	v_cndmask_b32_e64 v8, 0, 1, s[2:3]
	s_nop 0
	v_readfirstlane_b32 s2, v8
	s_bitcmp0_b32 s2, 0
	s_cbranch_scc0 .LBB4_45
	s_cmp_lt_i32 s28, 4
	s_cbranch_scc1 .LBB4_46
	s_cmp_gt_i32 s28, 4
	s_cbranch_scc0 .LBB4_47
	s_mov_b64 s[4:5], -1
	v_mov_b32_e32 v8, 0
	s_cmp_gt_i32 s28, 5
	v_mov_b32_e32 v167, 0
	v_mov_b32_e32 v166, 0
	v_mov_b32_e32 v165, 0
	v_mov_b32_e32 v164, 0
	v_mov_b32_e32 v162, 0
	v_mov_b32_e32 v160, 0
	v_mov_b32_e32 v159, 0
	v_mov_b32_e32 v157, 0
	v_mov_b32_e32 v151, 0
	v_mov_b32_e32 v149, 0
	v_mov_b32_e32 v147, 0
	v_mov_b32_e32 v146, 0
	v_mov_b32_e32 v144, 0
	v_mov_b32_e32 v143, 0
	v_mov_b32_e32 v152, 0
	v_mov_b32_e32 v153, 0
	v_mov_b32_e32 v154, 0
	v_mov_b32_e32 v155, 0
	v_mov_b32_e32 v156, 0
	v_mov_b32_e32 v158, 0
	v_mov_b32_e32 v161, 0
	v_mov_b32_e32 v163, 0
	v_mov_b32_e32 v168, 0
	v_mov_b32_e32 v169, 0
	v_mov_b32_e32 v170, 0
	v_mov_b32_e32 v171, 0
	v_mov_b32_e32 v172, 0
	v_mov_b32_e32 v173, 0
	v_mov_b32_e32 v174, 0
	v_mov_b32_e32 v145, 0
	v_mov_b32_e32 v148, 0
	v_mov_b32_e32 v150, 0
	s_cbranch_scc0 .LBB4_50
	s_cmp_eq_u32 s28, 6
	s_cbranch_scc0 .LBB4_49
	v_mov_b32_e32 v145, 0
	v_mov_b32_e32 v148, 0
	v_mov_b32_e32 v150, 0
	v_mov_b32_e32 v143, 0
	v_mov_b32_e32 v144, 0
	v_mov_b32_e32 v146, 0
	v_mov_b32_e32 v147, 0
	v_mov_b32_e32 v149, 0
	v_mov_b32_e32 v151, 0
	v_mov_b32_e32 v152, 0
	v_mov_b32_e32 v153, 0
	v_mov_b32_e32 v154, 0
	v_mov_b32_e32 v155, 0
	v_mov_b32_e32 v156, 0
	v_mov_b32_e32 v158, 0
	v_mov_b32_e32 v161, 0
	v_mov_b32_e32 v163, 0
	v_mov_b32_e32 v157, 0
	v_mov_b32_e32 v159, 0
	v_mov_b32_e32 v160, 0
	v_mov_b32_e32 v162, 0
	v_mov_b32_e32 v164, 0
	v_mov_b32_e32 v165, 0
	v_mov_b32_e32 v166, 0
	v_mov_b32_e32 v167, 0
	v_mov_b32_e32 v168, 0
	v_mov_b32_e32 v169, 0
	v_mov_b32_e32 v170, 0
	v_mov_b32_e32 v171, 0
	v_mov_b32_e32 v172, 0
	v_mov_b32_e32 v173, 0
	v_mov_b32_e32 v174, 0
	v_fma_mix_f32 v148, v43, v7, v148 op_sel_hi:[1,0,0]
	v_fma_mix_f32 v150, v45, v7, v150 op_sel_hi:[1,0,0]
	v_fma_mix_f32 v143, v50, v7, v143 op_sel_hi:[1,0,0]
	v_fma_mix_f32 v144, v54, v7, v144 op_sel_hi:[1,0,0]
	v_fma_mix_f32 v146, v58, v7, v146 op_sel_hi:[1,0,0]
	v_fma_mix_f32 v147, v61, v7, v147 op_sel_hi:[1,0,0]
	v_fma_mix_f32 v149, v64, v7, v149 op_sel_hi:[1,0,0]
	v_fma_mix_f32 v151, v66, v7, v151 op_sel_hi:[1,0,0]
	v_fma_mix_f32 v152, v43, v7, v152 op_sel:[1,0,0] op_sel_hi:[1,0,0]
	v_fma_mix_f32 v153, v45, v7, v153 op_sel:[1,0,0] op_sel_hi:[1,0,0]
	v_fma_mix_f32 v154, v50, v7, v154 op_sel:[1,0,0] op_sel_hi:[1,0,0]
	v_fma_mix_f32 v155, v54, v7, v155 op_sel:[1,0,0] op_sel_hi:[1,0,0]
	v_fma_mix_f32 v156, v58, v7, v156 op_sel:[1,0,0] op_sel_hi:[1,0,0]
	v_fma_mix_f32 v158, v61, v7, v158 op_sel:[1,0,0] op_sel_hi:[1,0,0]
	v_fma_mix_f32 v161, v64, v7, v161 op_sel:[1,0,0] op_sel_hi:[1,0,0]
	v_fma_mix_f32 v163, v66, v7, v163 op_sel:[1,0,0] op_sel_hi:[1,0,0]
	v_fma_mix_f32 v157, v72, v7, v157 op_sel_hi:[1,0,0]
	v_fma_mix_f32 v159, v76, v7, v159 op_sel_hi:[1,0,0]
	v_fma_mix_f32 v160, v83, v7, v160 op_sel_hi:[1,0,0]
	v_fma_mix_f32 v162, v85, v7, v162 op_sel_hi:[1,0,0]
	v_fma_mix_f32 v164, v89, v7, v164 op_sel_hi:[1,0,0]
	v_fma_mix_f32 v165, v92, v7, v165 op_sel_hi:[1,0,0]
	v_fma_mix_f32 v166, v95, v7, v166 op_sel_hi:[1,0,0]
	v_fma_mix_f32 v167, v96, v7, v167 op_sel_hi:[1,0,0]
	v_fma_mix_f32 v168, v72, v7, v168 op_sel:[1,0,0] op_sel_hi:[1,0,0]
	v_fma_mix_f32 v169, v76, v7, v169 op_sel:[1,0,0] op_sel_hi:[1,0,0]
	v_fma_mix_f32 v170, v83, v7, v170 op_sel:[1,0,0] op_sel_hi:[1,0,0]
	v_fma_mix_f32 v171, v85, v7, v171 op_sel:[1,0,0] op_sel_hi:[1,0,0]
	v_fma_mix_f32 v172, v89, v7, v172 op_sel:[1,0,0] op_sel_hi:[1,0,0]
	v_fma_mix_f32 v173, v92, v7, v173 op_sel:[1,0,0] op_sel_hi:[1,0,0]
	v_fma_mix_f32 v174, v95, v7, v174 op_sel:[1,0,0] op_sel_hi:[1,0,0]
	v_fma_mix_f32 v145, v96, v7, v145 op_sel:[1,0,0] op_sel_hi:[1,0,0]
	s_branch .LBB4_50

	.amdhsa_kernel _Z6k_iterILb0ELb1EEvPKfS1_PKiPK15HIP_vector_typeIfLj4EES7_S1_S1_S3_S1_PfS8_S1_S3_PDF16_PS5_SA_PiSA_SB_
		.amdhsa_group_segment_fixed_size 5808
		.amdhsa_private_segment_fixed_size 0
		.amdhsa_kernarg_size 152
		.amdhsa_user_sgpr_count 2
		.amdhsa_user_sgpr_dispatch_ptr 0
		.amdhsa_user_sgpr_queue_ptr 0
		.amdhsa_user_sgpr_kernarg_segment_ptr 1
		.amdhsa_user_sgpr_dispatch_id 0
		.amdhsa_user_sgpr_kernarg_preload_length 0
		.amdhsa_user_sgpr_kernarg_preload_offset 0
		.amdhsa_user_sgpr_private_segment_size 0
		.amdhsa_uses_dynamic_stack 0
		.amdhsa_enable_private_segment 0
		.amdhsa_system_sgpr_workgroup_id_x 1
		.amdhsa_system_sgpr_workgroup_id_y 0
		.amdhsa_system_sgpr_workgroup_id_z 0
		.amdhsa_system_sgpr_workgroup_info 0
		.amdhsa_system_vgpr_workitem_id 0
		.amdhsa_next_free_vgpr 184
		.amdhsa_next_free_sgpr 48
		.amdhsa_accum_offset 184
		.amdhsa_reserve_vcc 1
		.amdhsa_float_round_mode_32 0
		.amdhsa_float_round_mode_16_64 0
		.amdhsa_float_denorm_mode_32 3
		.amdhsa_float_denorm_mode_16_64 3
		.amdhsa_dx10_clamp 1
		.amdhsa_ieee_mode 1
		.amdhsa_fp16_overflow 0
		.amdhsa_tg_split 0
		.amdhsa_exception_fp_ieee_invalid_op 0
		.amdhsa_exception_fp_denorm_src 0
		.amdhsa_exception_fp_ieee_div_zero 0
		.amdhsa_exception_fp_ieee_overflow 0
		.amdhsa_exception_fp_ieee_underflow 0
		.amdhsa_exception_fp_ieee_inexact 0
		.amdhsa_exception_int_div_zero 0
	.end_amdhsa_kernel

amdhsa.kernels:
  - .agpr_count:     0
    .args:
      - .actual_access:  read_only
        .address_space:  global
        .offset:         0
        .size:           8
        .value_kind:     global_buffer
      - .actual_access:  read_only
        .address_space:  global
        .offset:         8
        .size:           8
        .value_kind:     global_buffer
      - .actual_access:  read_only
        .address_space:  global
        .offset:         16
        .size:           8
        .value_kind:     global_buffer
      - .actual_access:  read_only
        .address_space:  global
        .offset:         24
        .size:           8
        .value_kind:     global_buffer
      - .actual_access:  write_only
        .address_space:  global
        .offset:         32
        .size:           8
        .value_kind:     global_buffer
      - .actual_access:  write_only
        .address_space:  global
        .offset:         40
        .size:           8
        .value_kind:     global_buffer
      - .actual_access:  write_only
        .address_space:  global
        .offset:         48
        .size:           8
        .value_kind:     global_buffer
      - .actual_access:  write_only
        .address_space:  global
        .offset:         56
        .size:           8
        .value_kind:     global_buffer
      - .actual_access:  write_only
        .address_space:  global
        .offset:         64
        .size:           8
        .value_kind:     global_buffer
      - .actual_access:  write_only
        .address_space:  global
        .offset:         72
        .size:           8
        .value_kind:     global_buffer
      - .actual_access:  write_only
        .address_space:  global
        .offset:         80
        .size:           8
        .value_kind:     global_buffer
      - .actual_access:  write_only
        .address_space:  global
        .offset:         88
        .size:           8
        .value_kind:     global_buffer
      - .actual_access:  write_only
        .address_space:  global
        .offset:         96
        .size:           8
        .value_kind:     global_buffer
      - .actual_access:  write_only
        .address_space:  global
        .offset:         104
        .size:           8
        .value_kind:     global_buffer
      - .actual_access:  write_only
        .address_space:  global
        .offset:         112
        .size:           8
        .value_kind:     global_buffer
    .group_segment_fixed_size: 67584
    .kernarg_segment_align: 8
    .kernarg_segment_size: 120
    .language:       OpenCL C
    .language_version:
      - 2
      - 0
    .max_flat_workgroup_size: 1024
    .name:           _Z6k_sortPKfS0_PKiS2_PiP15HIP_vector_typeIfLj4EEPfS7_S3_S7_S7_S3_S3_S6_S6_
    .private_segment_fixed_size: 0
    .sgpr_count:     58
    .sgpr_spill_count: 0
    .symbol:         _Z6k_sortPKfS0_PKiS2_PiP15HIP_vector_typeIfLj4EEPfS7_S3_S7_S7_S3_S3_S6_S6_.kd
    .uniform_work_group_size: 1
    .uses_dynamic_stack: false
    .vgpr_count:     48
    .vgpr_spill_count: 0
    .wavefront_size: 64
  - .agpr_count:     0
    .args:
      - .actual_access:  read_only
        .address_space:  global
        .offset:         0
        .size:           8
        .value_kind:     global_buffer
      - .actual_access:  read_only
        .address_space:  global
        .offset:         8
        .size:           8
        .value_kind:     global_buffer
      - .actual_access:  read_only
        .address_space:  global
        .offset:         16
        .size:           8
        .value_kind:     global_buffer
      - .actual_access:  read_only
        .address_space:  global
        .offset:         24
        .size:           8
        .value_kind:     global_buffer
      - .actual_access:  read_only
        .address_space:  global
        .offset:         32
        .size:           8
        .value_kind:     global_buffer
      - .actual_access:  read_only
        .address_space:  global
        .offset:         40
        .size:           8
        .value_kind:     global_buffer
      - .actual_access:  read_only
        .address_space:  global
        .offset:         48
        .size:           8
        .value_kind:     global_buffer
      - .actual_access:  write_only
        .address_space:  global
        .offset:         56
        .size:           8
        .value_kind:     global_buffer
    .group_segment_fixed_size: 145952
    .kernarg_segment_align: 8
    .kernarg_segment_size: 64
    .language:       OpenCL C
    .language_version:
      - 2
      - 0
    .max_flat_workgroup_size: 512
    .name:           _Z7k_finalPK15HIP_vector_typeIfLj4EES2_PKiS4_PKfS6_PKDF16_Pf
    .private_segment_fixed_size: 0
    .sgpr_count:     34
    .sgpr_spill_count: 0
    .symbol:         _Z7k_finalPK15HIP_vector_typeIfLj4EES2_PKiS4_PKfS6_PKDF16_Pf.kd
    .uniform_work_group_size: 1
    .uses_dynamic_stack: false
    .vgpr_count:     177
    .vgpr_spill_count: 0
    .wavefront_size: 64
  - .agpr_count:     0
    .args:
      - .actual_access:  read_only
        .address_space:  global
        .offset:         0
        .size:           8
        .value_kind:     global_buffer
      - .actual_access:  read_only
        .address_space:  global
        .offset:         8
        .size:           8
        .value_kind:     global_buffer
      - .actual_access:  read_only
        .address_space:  global
        .offset:         16
        .size:           8
        .value_kind:     global_buffer
      - .actual_access:  read_only
        .address_space:  global
        .offset:         24
        .size:           8
        .value_kind:     global_buffer
      - .actual_access:  read_only
        .address_space:  global
        .offset:         32
        .size:           8
        .value_kind:     global_buffer
      - .actual_access:  read_only
        .address_space:  global
        .offset:         40
        .size:           8
        .value_kind:     global_buffer
      - .actual_access:  read_only
        .address_space:  global
        .offset:         48
        .size:           8
        .value_kind:     global_buffer
      - .actual_access:  read_only
        .address_space:  global
        .offset:         56
        .size:           8
        .value_kind:     global_buffer
      - .actual_access:  read_only
        .address_space:  global
        .offset:         64
        .size:           8
        .value_kind:     global_buffer
      - .address_space:  global
        .offset:         72
        .size:           8
        .value_kind:     global_buffer
      - .actual_access:  read_only
        .address_space:  global
        .offset:         80
        .size:           8
        .value_kind:     global_buffer
      - .actual_access:  read_only
        .address_space:  global
        .offset:         88
        .size:           8
        .value_kind:     global_buffer
      - .actual_access:  read_only
        .address_space:  global
        .offset:         96
        .size:           8
        .value_kind:     global_buffer
      - .actual_access:  write_only
        .address_space:  global
        .offset:         104
        .size:           8
        .value_kind:     global_buffer
      - .address_space:  global
        .offset:         112
        .size:           8
        .value_kind:     global_buffer
      - .actual_access:  write_only
        .address_space:  global
        .offset:         120
        .size:           8
        .value_kind:     global_buffer
      - .actual_access:  write_only
        .address_space:  global
        .offset:         128
        .size:           8
        .value_kind:     global_buffer
      - .actual_access:  write_only
        .address_space:  global
        .offset:         136
        .size:           8
        .value_kind:     global_buffer
      - .actual_access:  write_only
        .address_space:  global
        .offset:         144
        .size:           8
        .value_kind:     global_buffer
    .group_segment_fixed_size: 30384
    .kernarg_segment_align: 8
    .kernarg_segment_size: 152
    .language:       OpenCL C
    .language_version:
      - 2
      - 0
    .max_flat_workgroup_size: 512
    .name:           _Z6k_iterILb1ELb0EEvPKfS1_PKiPK15HIP_vector_typeIfLj4EES7_S1_S1_S3_S1_PfS8_S1_S3_PDF16_PS5_SA_PiSA_SB_
    .private_segment_fixed_size: 0
    .sgpr_count:     102
    .sgpr_spill_count: 0
    .symbol:         _Z6k_iterILb1ELb0EEvPKfS1_PKiPK15HIP_vector_typeIfLj4EES7_S1_S1_S3_S1_PfS8_S1_S3_PDF16_PS5_SA_PiSA_SB_.kd
    .uniform_work_group_size: 1
    .uses_dynamic_stack: false
    .vgpr_count:     216
    .vgpr_spill_count: 0
    .wavefront_size: 64
  - .agpr_count:     0
    .args:
      - .actual_access:  read_only
        .address_space:  global
        .offset:         0
        .size:           8
        .value_kind:     global_buffer
      - .actual_access:  read_only
        .address_space:  global
        .offset:         8
        .size:           8
        .value_kind:     global_buffer
      - .actual_access:  read_only
        .address_space:  global
        .offset:         16
        .size:           8
        .value_kind:     global_buffer
      - .actual_access:  read_only
        .address_space:  global
        .offset:         24
        .size:           8
        .value_kind:     global_buffer
      - .actual_access:  read_only
        .address_space:  global
        .offset:         32
        .size:           8
        .value_kind:     global_buffer
      - .actual_access:  read_only
        .address_space:  global
        .offset:         40
        .size:           8
        .value_kind:     global_buffer
      - .actual_access:  read_only
        .address_space:  global
        .offset:         48
        .size:           8
        .value_kind:     global_buffer
      - .actual_access:  read_only
        .address_space:  global
        .offset:         56
        .size:           8
        .value_kind:     global_buffer
      - .actual_access:  read_only
        .address_space:  global
        .offset:         64
        .size:           8
        .value_kind:     global_buffer
      - .address_space:  global
        .offset:         72
        .size:           8
        .value_kind:     global_buffer
      - .actual_access:  read_only
        .address_space:  global
        .offset:         80
        .size:           8
        .value_kind:     global_buffer
      - .actual_access:  read_only
        .address_space:  global
        .offset:         88
        .size:           8
        .value_kind:     global_buffer
      - .actual_access:  read_only
        .address_space:  global
        .offset:         96
        .size:           8
        .value_kind:     global_buffer
      - .actual_access:  read_only
        .address_space:  global
        .offset:         104
        .size:           8
        .value_kind:     global_buffer
      - .actual_access:  read_only
        .address_space:  global
        .offset:         112
        .size:           8
        .value_kind:     global_buffer
      - .actual_access:  read_only
        .address_space:  global
        .offset:         120
        .size:           8
        .value_kind:     global_buffer
      - .actual_access:  read_only
        .address_space:  global
        .offset:         128
        .size:           8
        .value_kind:     global_buffer
      - .actual_access:  read_only
        .address_space:  global
        .offset:         136
        .size:           8
        .value_kind:     global_buffer
      - .actual_access:  read_only
        .address_space:  global
        .offset:         144
        .size:           8
        .value_kind:     global_buffer
    .group_segment_fixed_size: 5808
    .kernarg_segment_align: 8
    .kernarg_segment_size: 152
    .language:       OpenCL C
    .language_version:
      - 2
      - 0
    .max_flat_workgroup_size: 512
    .name:           _Z6k_iterILb0ELb0EEvPKfS1_PKiPK15HIP_vector_typeIfLj4EES7_S1_S1_S3_S1_PfS8_S1_S3_PDF16_PS5_SA_PiSA_SB_
    .private_segment_fixed_size: 0
    .sgpr_count:     46
    .sgpr_spill_count: 0
    .symbol:         _Z6k_iterILb0ELb0EEvPKfS1_PKiPK15HIP_vector_typeIfLj4EES7_S1_S1_S3_S1_PfS8_S1_S3_PDF16_PS5_SA_PiSA_SB_.kd
    .uniform_work_group_size: 1
    .uses_dynamic_stack: false
    .vgpr_count:     184
    .vgpr_spill_count: 0
    .wavefront_size: 64
  - .agpr_count:     0
    .args:
      - .actual_access:  read_only
        .address_space:  global
        .offset:         0
        .size:           8
        .value_kind:     global_buffer
      - .actual_access:  read_only
        .address_space:  global
        .offset:         8
        .size:           8
        .value_kind:     global_buffer
      - .actual_access:  read_only
        .address_space:  global
        .offset:         16
        .size:           8
        .value_kind:     global_buffer
      - .actual_access:  read_only
        .address_space:  global
        .offset:         24
        .size:           8
        .value_kind:     global_buffer
      - .actual_access:  read_only
        .address_space:  global
        .offset:         32
        .size:           8
        .value_kind:     global_buffer
      - .actual_access:  read_only
        .address_space:  global
        .offset:         40
        .size:           8
        .value_kind:     global_buffer
      - .actual_access:  read_only
        .address_space:  global
        .offset:         48
        .size:           8
        .value_kind:     global_buffer
      - .actual_access:  read_only
        .address_space:  global
        .offset:         56
        .size:           8
        .value_kind:     global_buffer
      - .actual_access:  read_only
        .address_space:  global
        .offset:         64
        .size:           8
        .value_kind:     global_buffer
      - .address_space:  global
        .offset:         72
        .size:           8
        .value_kind:     global_buffer
      - .actual_access:  write_only
        .address_space:  global
        .offset:         80
        .size:           8
        .value_kind:     global_buffer
      - .actual_access:  read_only
        .address_space:  global
        .offset:         88
        .size:           8
        .value_kind:     global_buffer
      - .actual_access:  read_only
        .address_space:  global
        .offset:         96
        .size:           8
        .value_kind:     global_buffer
      - .actual_access:  read_only
        .address_space:  global
        .offset:         104
        .size:           8
        .value_kind:     global_buffer
      - .actual_access:  read_only
        .address_space:  global
        .offset:         112
        .size:           8
        .value_kind:     global_buffer
      - .actual_access:  read_only
        .address_space:  global
        .offset:         120
        .size:           8
        .value_kind:     global_buffer
      - .actual_access:  read_only
        .address_space:  global
        .offset:         128
        .size:           8
        .value_kind:     global_buffer
      - .actual_access:  read_only
        .address_space:  global
        .offset:         136
        .size:           8
        .value_kind:     global_buffer
      - .actual_access:  read_only
        .address_space:  global
        .offset:         144
        .size:           8
        .value_kind:     global_buffer
    .group_segment_fixed_size: 5808
    .kernarg_segment_align: 8
    .kernarg_segment_size: 152
    .language:       OpenCL C
    .language_version:
      - 2
      - 0
    .max_flat_workgroup_size: 512
    .name:           _Z6k_iterILb0ELb1EEvPKfS1_PKiPK15HIP_vector_typeIfLj4EES7_S1_S1_S3_S1_PfS8_S1_S3_PDF16_PS5_SA_PiSA_SB_
    .private_segment_fixed_size: 0
    .sgpr_count:     54
    .sgpr_spill_count: 0
    .symbol:         _Z6k_iterILb0ELb1EEvPKfS1_PKiPK15HIP_vector_typeIfLj4EES7_S1_S1_S3_S1_PfS8_S1_S3_PDF16_PS5_SA_PiSA_SB_.kd
    .uniform_work_group_size: 1
    .uses_dynamic_stack: false
    .vgpr_count:     184
    .vgpr_spill_count: 0
    .wavefront_size: 64
